# v7 with glc on the two scalar expert-lookup loads (always served from L2)
# baseline (speedup 1.0000x reference)
.LBB0_1406:
	s_andn2_b64 vcc, exec, s[18:19]
	s_cbranch_vccnz .LBB0_1408
	s_ashr_i32 s2, s4, 31
	s_lshr_b32 s2, s2, 29
	s_add_i32 s2, s4, s2
	s_ashr_i32 s5, s2, 3
	s_and_b32 s2, s2, -8
	s_sub_i32 s2, s4, s2
	s_cmp_lt_i32 s2, 0
	s_cselect_b32 s4, s46, s45
	s_mul_i32 s2, s4, s2
	s_add_i32 s2, s2, s5
	s_mul_hi_i32 s4, s2, 0x92492493
	s_add_i32 s4, s4, s2
	s_lshr_b32 s5, s4, 31
	s_ashr_i32 s4, s4, 8
	s_add_i32 s4, s4, s5
	s_lshl_b32 s5, s4, 3
	s_sub_i32 s14, s38, s5
	s_min_i32 s15, s14, 8
	s_abs_i32 s14, s15
	v_cvt_f32_u32_e32 v0, s14
	s_sub_i32 s17, 0, s14
	s_mulk_i32 s4, 0x1c0
	s_sub_i32 s2, s2, s4
	v_rcp_iflag_f32_e32 v0, v0
	s_abs_i32 s4, s2
	s_xor_b32 s16, s2, s15
	s_ashr_i32 s16, s16, 31
	v_mul_f32_e32 v0, 0x4f7ffffe, v0
	v_cvt_u32_f32_e32 v0, v0
	s_nop 0
	v_readfirstlane_b32 s18, v0
	s_mul_i32 s17, s17, s18
	s_mul_hi_u32 s17, s18, s17
	s_add_i32 s18, s18, s17
	s_mul_hi_u32 s17, s4, s18
	s_mul_i32 s18, s17, s14
	s_sub_i32 s4, s4, s18
	s_add_i32 s19, s17, 1
	s_sub_i32 s18, s4, s14
	s_cmp_ge_u32 s4, s14
	s_cselect_b32 s17, s19, s17
	s_cselect_b32 s4, s18, s4
	s_add_i32 s18, s17, 1
	s_cmp_ge_u32 s4, s14
	s_cselect_b32 s4, s18, s17
	s_xor_b32 s4, s4, s16
	s_sub_i32 s14, s4, s16
	s_mul_i32 s4, s14, s15
	s_sub_i32 s2, s2, s4
	s_add_i32 s16, s2, s5
	s_ashr_i32 s17, s16, 31
	s_lshl_b64 s[4:5], s[16:17], 2
	s_add_u32 s4, s43, s4
	s_addc_u32 s5, s44, s5
	s_load_dword s53, s[4:5], 0x0 glc
	s_waitcnt lgkmcnt(0)

.LBB0_1481:
	s_add_i32 s45, s45, 1
	s_mul_i32 s4, s45, s46
	s_mul_hi_u32 s5, s45, s33
	s_add_i32 s5, s5, s4
	s_mul_i32 s4, s45, s33
	s_add_u32 s4, s4, s87
	s_addc_u32 s5, s5, s47
	v_cmp_ge_i64_e32 vcc, s[4:5], v[128:129]
	v_cmp_lt_i64_e64 s[6:7], s[4:5], v[128:129]
	s_cbranch_vccnz .LBB0_1483
	s_ashr_i32 s5, s4, 31
	s_lshr_b32 s5, s5, 29
	s_add_i32 s5, s4, s5
	s_ashr_i32 s18, s5, 3
	s_and_b32 s5, s5, -8
	s_sub_i32 s4, s4, s5
	s_lshr_b32 s5, s4, 31
	s_add_i32 s5, s3, s5
	s_mul_i32 s4, s5, s4
	s_add_i32 s4, s4, s18
	s_ashr_i32 s5, s4, 31
	s_lshr_b32 s5, s5, 26
	s_add_i32 s5, s4, s5
	s_ashr_i32 s18, s5, 6
	s_lshl_b32 s18, s18, 3
	s_sub_i32 s19, s3, s18
	s_min_i32 s19, s19, 8
	s_abs_i32 s20, s19
	v_cvt_f32_u32_e32 v0, s20
	s_sub_i32 s23, 0, s20
	s_andn2_b32 s5, s5, 63
	s_sub_i32 s4, s4, s5
	v_rcp_iflag_f32_e32 v0, v0
	s_abs_i32 s5, s4
	s_xor_b32 s21, s4, s19
	s_ashr_i32 s21, s21, 31
	v_mul_f32_e32 v0, 0x4f7ffffe, v0
	v_cvt_u32_f32_e32 v0, v0
	s_nop 0
	v_readfirstlane_b32 s26, v0
	s_mul_i32 s23, s23, s26
	s_mul_hi_u32 s23, s26, s23
	s_add_i32 s26, s26, s23
	s_mul_hi_u32 s23, s5, s26
	s_mul_i32 s26, s23, s20
	s_sub_i32 s5, s5, s26
	s_add_i32 s27, s23, 1
	s_sub_i32 s26, s5, s20
	s_cmp_ge_u32 s5, s20
	s_cselect_b32 s23, s27, s23
	s_cselect_b32 s5, s26, s5
	s_add_i32 s26, s23, 1
	s_cmp_ge_u32 s5, s20
	s_cselect_b32 s5, s26, s23
	s_xor_b32 s5, s5, s21
	s_sub_i32 s50, s5, s21
	s_mul_i32 s5, s50, s19
	s_sub_i32 s4, s4, s5
	s_add_i32 s18, s4, s18
	s_ashr_i32 s19, s18, 31
	s_lshl_b64 s[4:5], s[18:19], 2
	s_add_u32 s4, s38, s4
	s_addc_u32 s5, s39, s5
	s_load_dword s19, s[4:5], 0x0 glc
	s_waitcnt lgkmcnt(0)
